# inline-0.5 attention srcC + moe_tables loads batched + gmlp unit loads batched
# speedup vs baseline: 1.0086x; 1.0048x over previous
.LBB0_407:
	s_ashr_i32 s15, s4, 2
	s_mul_hi_i32 s25, s15, 0x78787879
	s_lshr_b32 s26, s25, 31
	s_ashr_i32 s25, s25, 4
	s_add_i32 s25, s25, s26
	s_mul_i32 s26, s25, 0xffffffde
	s_add_i32 s26, s26, s15
	s_ashr_i32 s27, s26, 31
	s_mul_hi_i32 s15, s25, 0x1100
	s_mulk_i32 s25, 0x1100
	s_lshl_b64 s[26:27], s[26:27], 7
	s_add_u32 s38, s26, s25
	s_addc_u32 s39, s27, s15
	s_lshl_b64 s[26:27], s[38:39], 9
	s_add_u32 s26, s13, s26
	s_addc_u32 s27, s14, s27
	v_lshl_add_u64 v[148:149], s[26:27], 0, v[16:17]
	v_lshl_add_u64 v[150:151], s[26:27], 0, v[18:19]
	v_lshl_add_u64 v[148:149], v[148:149], 0, v[112:113]
	v_lshl_add_u64 v[150:151], v[150:151], 0, v[112:113]
	v_lshl_add_u64 v[28:29], s[38:39], 0, v[20:21]
	global_load_dwordx4 v[66:69], v[148:149], off
	global_load_dwordx4 v[70:73], v[150:151], off
	v_lshlrev_b64 v[28:29], 9, v[28:29]
	global_load_dwordx4 v[74:77], v[22:23], off
	global_load_dwordx4 v[78:81], v[22:23], off offset:32
	global_load_dwordx4 v[82:85], v[22:23], off offset:64
	global_load_dwordx4 v[86:89], v[22:23], off offset:96
	global_load_dwordx4 v[90:93], v[22:23], off offset:128
	global_load_dwordx4 v[94:97], v[22:23], off offset:160
	global_load_dwordx4 v[98:101], v[22:23], off offset:192
	global_load_dwordx4 v[102:105], v[22:23], off offset:224
	v_lshl_add_u64 v[28:29], v[26:27], 0, v[28:29]
	global_load_dword v30, v[24:25], off
	v_mov_b64_e32 v[42:43], s[86:87]
	global_load_dwordx2 v[106:107], v[28:29], off
	global_load_dwordx2 v[108:109], v[28:29], off offset:16
	global_load_dwordx2 v[110:111], v[28:29], off offset:32
	global_load_dwordx2 v[114:115], v[28:29], off offset:48
	s_add_i32 s15, s4, 0x100
	s_cmpk_gt_i32 s4, 0x77f
	s_mov_b32 s4, s15
	s_barrier
	s_waitcnt vmcnt(13)
	ds_write_b128 v31, v[66:69]
	ds_write_b128 v40, v[70:73]
	s_waitcnt lgkmcnt(0)
	s_barrier
	ds_read_b64_tr_b16 v[116:117], v41
	ds_read_b64_tr_b16 v[118:119], v41 offset:768
	ds_read_b64_tr_b16 v[120:121], v41 offset:3072
	ds_read_b64_tr_b16 v[122:123], v41 offset:3840
	ds_read_b64_tr_b16 v[124:125], v41 offset:6144
	ds_read_b64_tr_b16 v[126:127], v41 offset:6912
	ds_read_b64_tr_b16 v[128:129], v41 offset:9216
	ds_read_b64_tr_b16 v[130:131], v41 offset:9984
	ds_read_b64_tr_b16 v[132:133], v41 offset:12288
	ds_read_b64_tr_b16 v[134:135], v41 offset:13056
	ds_read_b64_tr_b16 v[136:137], v41 offset:15360
	ds_read_b64_tr_b16 v[138:139], v41 offset:16128
	ds_read_b64_tr_b16 v[140:141], v41 offset:18432
	ds_read_b64_tr_b16 v[142:143], v41 offset:19200
	s_waitcnt vmcnt(12) lgkmcnt(12)
	v_mfma_f32_32x32x16_bf16 v[0:15], v[116:119], v[74:77], 0
	ds_read_b64_tr_b16 v[144:145], v41 offset:21504
	ds_read_b64_tr_b16 v[146:147], v41 offset:22272
	s_waitcnt vmcnt(11) lgkmcnt(12)
	v_mfma_f32_32x32x16_bf16 v[0:15], v[120:123], v[78:81], v[0:15]
	s_waitcnt vmcnt(10) lgkmcnt(10)
	v_mfma_f32_32x32x16_bf16 v[0:15], v[124:127], v[82:85], v[0:15]
	s_waitcnt vmcnt(9) lgkmcnt(8)
	v_mfma_f32_32x32x16_bf16 v[0:15], v[128:131], v[86:89], v[0:15]
	s_waitcnt vmcnt(8) lgkmcnt(6)
	v_mfma_f32_32x32x16_bf16 v[0:15], v[132:135], v[90:93], v[0:15]
	s_waitcnt vmcnt(7) lgkmcnt(4)
	v_mfma_f32_32x32x16_bf16 v[0:15], v[136:139], v[94:97], v[0:15]
	s_waitcnt vmcnt(6) lgkmcnt(2)
	v_mfma_f32_32x32x16_bf16 v[0:15], v[140:143], v[98:101], v[0:15]
	s_waitcnt vmcnt(5) lgkmcnt(0)
	v_mfma_f32_32x32x16_bf16 v[0:15], v[144:147], v[102:105], v[0:15]
	s_waitcnt vmcnt(0)
	s_nop 8
	v_mov_b32_e32 v32, v106
	v_mov_b32_e32 v33, v107
	v_pk_add_f32 v[0:1], v[0:1], v[30:31] op_sel_hi:[1,0]
	v_pk_add_f32 v[2:3], v[2:3], v[30:31] op_sel_hi:[1,0]
	v_pk_add_f32 v[4:5], v[4:5], v[30:31] op_sel_hi:[1,0]
	v_lshlrev_b32_e32 v34, 16, v32
	v_and_b32_e32 v35, 0xffff0000, v32
	v_fma_f32 v32, |v34|, s29, 1.0
	v_pk_mul_f32 v[36:37], v[34:35], v[34:35]
	v_rcp_f32_e32 v38, v32
	v_mul_f32_e32 v32, 0xbf38aa3b, v36
	v_exp_f32_e32 v36, v32
	v_fma_f32 v32, |v35|, s29, 1.0
	v_rcp_f32_e32 v39, v32
	v_mul_f32_e32 v32, 0xbf38aa3b, v37
	v_exp_f32_e32 v37, v32
	v_cmp_gt_f32_e32 vcc, 0, v34
	v_pk_fma_f32 v[44:45], v[38:39], s[82:83], v[42:43] op_sel_hi:[1,0,0]
	v_cmp_gt_f32_e64 s[38:39], 0, v35
	v_pk_fma_f32 v[44:45], v[38:39], v[44:45], s[96:97] op_sel_hi:[1,1,0]
	v_lshlrev_b32_e32 v32, 16, v33
	v_pk_fma_f32 v[44:45], v[38:39], v[44:45], s[28:29] op_sel_hi:[1,1,0]
	v_and_b32_e32 v33, 0xffff0000, v33
	v_pk_fma_f32 v[44:45], v[38:39], v[44:45], s[30:31] op_sel_hi:[1,1,0]
	s_nop 0
	v_pk_mul_f32 v[38:39], v[38:39], v[44:45]
	s_nop 0
	v_pk_mul_f32 v[36:37], v[36:37], v[38:39]
	s_nop 0
	v_pk_mul_f32 v[38:39], v[36:37], v[34:35]
	v_pk_fma_f32 v[34:35], v[36:37], v[34:35], v[34:35] neg_lo:[1,0,0] neg_hi:[1,0,0]
	v_pk_mul_f32 v[36:37], v[32:33], v[32:33]
	v_cndmask_b32_e64 v35, v35, v39, s[38:39]
	v_cndmask_b32_e32 v34, v34, v38, vcc
	v_pk_mul_f32 v[0:1], v[0:1], v[34:35]
	v_cmp_gt_f32_e32 vcc, 0, v32
	v_cvt_pk_bf16_f32 v0, v0, v1
	v_fma_f32 v1, |v32|, s29, 1.0
	v_rcp_f32_e32 v34, v1
	v_mul_f32_e32 v1, 0xbf38aa3b, v36
	v_exp_f32_e32 v36, v1
	v_fma_f32 v1, |v33|, s29, 1.0
	v_rcp_f32_e32 v35, v1
	v_mul_f32_e32 v1, 0xbf38aa3b, v37
	v_exp_f32_e32 v37, v1
	v_cmp_gt_f32_e64 s[38:39], 0, v33
	v_pk_fma_f32 v[38:39], v[34:35], s[82:83], v[42:43] op_sel_hi:[1,0,0]
	s_nop 0
	v_pk_fma_f32 v[38:39], v[34:35], v[38:39], s[96:97] op_sel_hi:[1,1,0]
	s_nop 0
	v_pk_fma_f32 v[38:39], v[34:35], v[38:39], s[28:29] op_sel_hi:[1,1,0]
	s_nop 0
	v_pk_fma_f32 v[38:39], v[34:35], v[38:39], s[30:31] op_sel_hi:[1,1,0]
	s_nop 0
	v_pk_mul_f32 v[34:35], v[34:35], v[38:39]
	s_nop 0
	v_pk_mul_f32 v[34:35], v[36:37], v[34:35]
	s_nop 0
	v_pk_mul_f32 v[36:37], v[34:35], v[32:33]
	v_pk_fma_f32 v[32:33], v[34:35], v[32:33], v[32:33] neg_lo:[1,0,0] neg_hi:[1,0,0]
	s_nop 0
	v_cndmask_b32_e64 v33, v33, v37, s[38:39]
	v_cndmask_b32_e32 v32, v32, v36, vcc
	v_pk_mul_f32 v[2:3], v[2:3], v[32:33]
	s_nop 0
	v_cvt_pk_bf16_f32 v1, v2, v3
	global_store_dwordx2 v[28:29], v[0:1], off
	s_nop 1
	v_mov_b32_e32 v0, v108
	v_mov_b32_e32 v1, v109
	v_lshlrev_b32_e32 v2, 16, v0
	v_and_b32_e32 v3, 0xffff0000, v0
	v_fma_f32 v0, |v2|, s29, 1.0
	v_pk_mul_f32 v[34:35], v[2:3], v[2:3]
	v_rcp_f32_e32 v32, v0
	v_mul_f32_e32 v0, 0xbf38aa3b, v34
	v_exp_f32_e32 v34, v0
	v_fma_f32 v0, |v3|, s29, 1.0
	v_rcp_f32_e32 v33, v0
	v_mul_f32_e32 v0, 0xbf38aa3b, v35
	v_exp_f32_e32 v35, v0
	v_cmp_gt_f32_e32 vcc, 0, v2
	v_pk_fma_f32 v[36:37], v[32:33], s[82:83], v[42:43] op_sel_hi:[1,0,0]
	v_cmp_gt_f32_e64 s[38:39], 0, v3
	v_pk_fma_f32 v[36:37], v[32:33], v[36:37], s[96:97] op_sel_hi:[1,1,0]
	s_nop 0
	v_pk_fma_f32 v[36:37], v[32:33], v[36:37], s[28:29] op_sel_hi:[1,1,0]
	s_nop 0
	v_pk_fma_f32 v[36:37], v[32:33], v[36:37], s[30:31] op_sel_hi:[1,1,0]
	s_nop 0
	v_pk_mul_f32 v[32:33], v[32:33], v[36:37]
	s_nop 0
	v_pk_mul_f32 v[32:33], v[34:35], v[32:33]
	s_nop 0
	v_pk_mul_f32 v[34:35], v[32:33], v[2:3]
	v_pk_fma_f32 v[2:3], v[32:33], v[2:3], v[2:3] neg_lo:[1,0,0] neg_hi:[1,0,0]
	s_nop 0
	v_cndmask_b32_e64 v3, v3, v35, s[38:39]
	v_cndmask_b32_e32 v2, v2, v34, vcc
	v_pk_mul_f32 v[2:3], v[4:5], v[2:3]
	s_nop 0
	v_cvt_pk_bf16_f32 v0, v2, v3
	v_lshlrev_b32_e32 v2, 16, v1
	v_and_b32_e32 v3, 0xffff0000, v1
	v_fma_f32 v1, |v2|, s29, 1.0
	v_pk_mul_f32 v[32:33], v[2:3], v[2:3]
	v_rcp_f32_e32 v4, v1
	v_mul_f32_e32 v1, 0xbf38aa3b, v32
	v_exp_f32_e32 v32, v1
	v_fma_f32 v1, |v3|, s29, 1.0
	v_rcp_f32_e32 v5, v1
	v_mul_f32_e32 v1, 0xbf38aa3b, v33
	v_exp_f32_e32 v33, v1
	v_cmp_gt_f32_e32 vcc, 0, v2
	v_pk_fma_f32 v[34:35], v[4:5], s[82:83], v[42:43] op_sel_hi:[1,0,0]
	v_cmp_gt_f32_e64 s[38:39], 0, v3
	v_pk_fma_f32 v[34:35], v[4:5], v[34:35], s[96:97] op_sel_hi:[1,1,0]
	s_nop 0
	v_pk_fma_f32 v[34:35], v[4:5], v[34:35], s[28:29] op_sel_hi:[1,1,0]
	s_nop 0
	v_pk_fma_f32 v[34:35], v[4:5], v[34:35], s[30:31] op_sel_hi:[1,1,0]
	s_nop 0
	v_pk_mul_f32 v[4:5], v[4:5], v[34:35]
	s_nop 0
	v_pk_mul_f32 v[4:5], v[32:33], v[4:5]
	s_nop 0
	v_pk_mul_f32 v[32:33], v[4:5], v[2:3]
	v_pk_fma_f32 v[2:3], v[4:5], v[2:3], v[2:3] neg_lo:[1,0,0] neg_hi:[1,0,0]
	v_pk_add_f32 v[4:5], v[6:7], v[30:31] op_sel_hi:[1,0]
	v_cndmask_b32_e64 v3, v3, v33, s[38:39]
	v_cndmask_b32_e32 v2, v2, v32, vcc
	v_pk_mul_f32 v[2:3], v[4:5], v[2:3]
	s_nop 0
	v_cvt_pk_bf16_f32 v1, v2, v3
	global_store_dwordx2 v[28:29], v[0:1], off offset:16
	s_nop 1
	v_mov_b32_e32 v0, v110
	v_mov_b32_e32 v1, v111
	v_lshlrev_b32_e32 v2, 16, v0
	v_and_b32_e32 v3, 0xffff0000, v0
	v_fma_f32 v0, |v2|, s29, 1.0
	v_pk_mul_f32 v[6:7], v[2:3], v[2:3]
	v_rcp_f32_e32 v4, v0
	v_mul_f32_e32 v0, 0xbf38aa3b, v6
	v_exp_f32_e32 v6, v0
	v_fma_f32 v0, |v3|, s29, 1.0
	v_rcp_f32_e32 v5, v0
	v_mul_f32_e32 v0, 0xbf38aa3b, v7
	v_exp_f32_e32 v7, v0
	v_cmp_gt_f32_e32 vcc, 0, v2
	v_pk_fma_f32 v[32:33], v[4:5], s[82:83], v[42:43] op_sel_hi:[1,0,0]
	v_cmp_gt_f32_e64 s[38:39], 0, v3
	v_pk_fma_f32 v[32:33], v[4:5], v[32:33], s[96:97] op_sel_hi:[1,1,0]
	s_nop 0
	v_pk_fma_f32 v[32:33], v[4:5], v[32:33], s[28:29] op_sel_hi:[1,1,0]
	s_nop 0
	v_pk_fma_f32 v[32:33], v[4:5], v[32:33], s[30:31] op_sel_hi:[1,1,0]
	s_nop 0
	v_pk_mul_f32 v[4:5], v[4:5], v[32:33]
	s_nop 0
	v_pk_mul_f32 v[4:5], v[6:7], v[4:5]
	s_nop 0
	v_pk_mul_f32 v[6:7], v[4:5], v[2:3]
	v_pk_fma_f32 v[2:3], v[4:5], v[2:3], v[2:3] neg_lo:[1,0,0] neg_hi:[1,0,0]
	v_pk_add_f32 v[4:5], v[8:9], v[30:31] op_sel_hi:[1,0]
	v_cndmask_b32_e64 v3, v3, v7, s[38:39]
	v_cndmask_b32_e32 v2, v2, v6, vcc
	v_pk_mul_f32 v[2:3], v[4:5], v[2:3]
	s_nop 0
	v_cvt_pk_bf16_f32 v0, v2, v3
	v_lshlrev_b32_e32 v2, 16, v1
	v_and_b32_e32 v3, 0xffff0000, v1
	v_fma_f32 v1, |v2|, s29, 1.0
	v_pk_mul_f32 v[6:7], v[2:3], v[2:3]
	v_rcp_f32_e32 v4, v1
	v_mul_f32_e32 v1, 0xbf38aa3b, v6
	v_exp_f32_e32 v6, v1
	v_fma_f32 v1, |v3|, s29, 1.0
	v_rcp_f32_e32 v5, v1
	v_mul_f32_e32 v1, 0xbf38aa3b, v7
	v_exp_f32_e32 v7, v1
	v_cmp_gt_f32_e32 vcc, 0, v2
	v_pk_fma_f32 v[8:9], v[4:5], s[82:83], v[42:43] op_sel_hi:[1,0,0]
	v_cmp_gt_f32_e64 s[38:39], 0, v3
	v_pk_fma_f32 v[8:9], v[4:5], v[8:9], s[96:97] op_sel_hi:[1,1,0]
	s_nop 0
	v_pk_fma_f32 v[8:9], v[4:5], v[8:9], s[28:29] op_sel_hi:[1,1,0]
	s_nop 0
	v_pk_fma_f32 v[8:9], v[4:5], v[8:9], s[30:31] op_sel_hi:[1,1,0]
	s_nop 0
	v_pk_mul_f32 v[4:5], v[4:5], v[8:9]
	s_nop 0
	v_pk_mul_f32 v[4:5], v[6:7], v[4:5]
	s_nop 0
	v_pk_mul_f32 v[6:7], v[4:5], v[2:3]
	v_pk_fma_f32 v[2:3], v[4:5], v[2:3], v[2:3] neg_lo:[1,0,0] neg_hi:[1,0,0]
	v_pk_add_f32 v[4:5], v[10:11], v[30:31] op_sel_hi:[1,0]
	v_cndmask_b32_e64 v3, v3, v7, s[38:39]
	v_cndmask_b32_e32 v2, v2, v6, vcc
	v_pk_mul_f32 v[2:3], v[4:5], v[2:3]
	s_nop 0
	v_cvt_pk_bf16_f32 v1, v2, v3
	global_store_dwordx2 v[28:29], v[0:1], off offset:32
	s_nop 1
	v_mov_b32_e32 v0, v114
	v_mov_b32_e32 v1, v115
	v_lshlrev_b32_e32 v2, 16, v0
	v_and_b32_e32 v3, 0xffff0000, v0
	v_fma_f32 v0, |v2|, s29, 1.0
	v_pk_mul_f32 v[6:7], v[2:3], v[2:3]
	v_rcp_f32_e32 v4, v0
	v_mul_f32_e32 v0, 0xbf38aa3b, v6
	v_exp_f32_e32 v6, v0
	v_fma_f32 v0, |v3|, s29, 1.0
	v_rcp_f32_e32 v5, v0
	v_mul_f32_e32 v0, 0xbf38aa3b, v7
	v_exp_f32_e32 v7, v0
	v_cmp_gt_f32_e32 vcc, 0, v2
	v_pk_fma_f32 v[8:9], v[4:5], s[82:83], v[42:43] op_sel_hi:[1,0,0]
	v_cmp_gt_f32_e64 s[38:39], 0, v3
	v_pk_fma_f32 v[8:9], v[4:5], v[8:9], s[96:97] op_sel_hi:[1,1,0]
	s_nop 0
	v_pk_fma_f32 v[8:9], v[4:5], v[8:9], s[28:29] op_sel_hi:[1,1,0]
	s_nop 0
	v_pk_fma_f32 v[8:9], v[4:5], v[8:9], s[30:31] op_sel_hi:[1,1,0]
	s_nop 0
	v_pk_mul_f32 v[4:5], v[4:5], v[8:9]
	s_nop 0
	v_pk_mul_f32 v[4:5], v[6:7], v[4:5]
	s_nop 0
	v_pk_mul_f32 v[6:7], v[4:5], v[2:3]
	v_pk_fma_f32 v[2:3], v[4:5], v[2:3], v[2:3] neg_lo:[1,0,0] neg_hi:[1,0,0]
	v_pk_add_f32 v[4:5], v[12:13], v[30:31] op_sel_hi:[1,0]
	v_cndmask_b32_e64 v3, v3, v7, s[38:39]
	v_cndmask_b32_e32 v2, v2, v6, vcc
	v_pk_mul_f32 v[2:3], v[4:5], v[2:3]
	s_nop 0
	v_cvt_pk_bf16_f32 v0, v2, v3
	v_lshlrev_b32_e32 v2, 16, v1
	v_and_b32_e32 v3, 0xffff0000, v1
	v_fma_f32 v1, |v2|, s29, 1.0
	v_pk_mul_f32 v[6:7], v[2:3], v[2:3]
	v_rcp_f32_e32 v4, v1
	v_mul_f32_e32 v1, 0xbf38aa3b, v6
	v_exp_f32_e32 v6, v1
	v_fma_f32 v1, |v3|, s29, 1.0
	v_rcp_f32_e32 v5, v1
	v_mul_f32_e32 v1, 0xbf38aa3b, v7
	v_exp_f32_e32 v7, v1
	v_cmp_gt_f32_e32 vcc, 0, v2
	v_pk_fma_f32 v[8:9], v[4:5], s[82:83], v[42:43] op_sel_hi:[1,0,0]
	v_cmp_gt_f32_e64 s[38:39], 0, v3
	v_pk_fma_f32 v[8:9], v[4:5], v[8:9], s[96:97] op_sel_hi:[1,1,0]
	s_nop 0
	v_pk_fma_f32 v[8:9], v[4:5], v[8:9], s[28:29] op_sel_hi:[1,1,0]
	s_nop 0
	v_pk_fma_f32 v[8:9], v[4:5], v[8:9], s[30:31] op_sel_hi:[1,1,0]
	s_nop 0
	v_pk_mul_f32 v[4:5], v[4:5], v[8:9]
	s_nop 0
	v_pk_mul_f32 v[4:5], v[6:7], v[4:5]
	s_nop 0
	v_pk_mul_f32 v[6:7], v[4:5], v[2:3]
	v_pk_fma_f32 v[2:3], v[4:5], v[2:3], v[2:3] neg_lo:[1,0,0] neg_hi:[1,0,0]
	v_pk_add_f32 v[4:5], v[14:15], v[30:31] op_sel_hi:[1,0]
	v_cndmask_b32_e64 v3, v3, v7, s[38:39]
	v_cndmask_b32_e32 v2, v2, v6, vcc
	v_pk_mul_f32 v[2:3], v[4:5], v[2:3]
	s_nop 0
	v_cvt_pk_bf16_f32 v1, v2, v3
	global_store_dwordx2 v[28:29], v[0:1], off offset:48
	s_cbranch_scc0 .LBB0_407

.LBB0_1005:
	s_andn2_b64 vcc, exec, s[6:7]
	s_cbranch_vccnz .LBB0_1068
	s_mov_b32 s12, s34
	s_mov_b32 s2, s31
	v_mbcnt_lo_u32_b32 v1, -1, 0
	v_mbcnt_hi_u32_b32 v1, -1, v1
	s_waitcnt vmcnt(0) lgkmcnt(0)
	v_lshl_add_u32 v0, s12, 6, v1
	v_cmp_eq_u32_e32 vcc, 0, v0
	s_barrier
	s_and_saveexec_b64 s[6:7], vcc
	s_cbranch_execz .LBB0_1008
	v_readlane_b32 s14, v255, 20
	v_readlane_b32 s15, v255, 21
	s_lshl_b32 s4, s14, 5
	s_lshl_b64 s[14:15], s[4:5], 2
	v_readlane_b32 s4, v254, 22
	s_add_u32 s26, s4, s14
	v_readlane_b32 s4, v254, 23
	s_addc_u32 s27, s4, s15
	v_readlane_b32 s4, v254, 48
	v_mov_b32_e32 v3, s97
	s_nop 0
	v_mov_b32_e32 v2, s4
	ds_write_b32 v2, v113
	global_load_dwordx4 v[32:35], v113, s[26:27] offset:0 sc1
	global_load_dwordx4 v[36:39], v113, s[26:27] offset:16 sc1
	global_load_dwordx4 v[40:43], v113, s[26:27] offset:32 sc1
	global_load_dwordx4 v[44:47], v113, s[26:27] offset:48 sc1
	global_load_dwordx4 v[48:51], v113, s[26:27] offset:64 sc1
	global_load_dwordx4 v[52:55], v113, s[26:27] offset:80 sc1
	global_load_dwordx4 v[56:59], v113, s[26:27] offset:96 sc1
	global_load_dwordx4 v[60:63], v113, s[26:27] offset:112 sc1
	s_waitcnt vmcnt(0)
	v_mov_b32_e32 v2, v32
	v_readlane_b32 s4, v254, 49
	v_add_u32_e32 v2, 0xff, v2
	v_and_b32_e32 v2, 0xffffff00, v2
	ds_write_b32 v3, v2
	v_mov_b32_e32 v3, v33
	v_add_u32_e32 v3, 0xff, v3
	v_and_b32_e32 v3, 0xffffff00, v3
	v_add_u32_e32 v2, v3, v2
	v_mov_b32_e32 v3, s4
	ds_write_b32 v3, v2
	v_mov_b32_e32 v3, v34
	v_readlane_b32 s4, v254, 50
	v_add_u32_e32 v3, 0xff, v3
	v_and_b32_e32 v3, 0xffffff00, v3
	v_add_u32_e32 v2, v3, v2
	v_mov_b32_e32 v3, s69
	ds_write_b32 v3, v2
	v_mov_b32_e32 v3, v35
	v_add_u32_e32 v3, 0xff, v3
	v_and_b32_e32 v3, 0xffffff00, v3
	v_add_u32_e32 v2, v3, v2
	v_mov_b32_e32 v3, s4
	ds_write_b32 v3, v2
	v_mov_b32_e32 v3, v36
	v_readlane_b32 s4, v254, 51
	v_add_u32_e32 v3, 0xff, v3
	v_and_b32_e32 v3, 0xffffff00, v3
	v_add_u32_e32 v2, v3, v2
	v_mov_b32_e32 v3, s36
	ds_write_b32 v3, v2
	v_mov_b32_e32 v3, v37
	v_add_u32_e32 v3, 0xff, v3
	v_and_b32_e32 v3, 0xffffff00, v3
	v_add_u32_e32 v2, v3, v2
	v_mov_b32_e32 v3, s4
	ds_write_b32 v3, v2
	v_mov_b32_e32 v3, v38
	v_readlane_b32 s4, v254, 52
	v_add_u32_e32 v3, 0xff, v3
	v_and_b32_e32 v3, 0xffffff00, v3
	v_add_u32_e32 v2, v3, v2
	v_mov_b32_e32 v3, s83
	ds_write_b32 v3, v2
	v_mov_b32_e32 v3, v39
	v_add_u32_e32 v3, 0xff, v3
	v_and_b32_e32 v3, 0xffffff00, v3
	v_add_u32_e32 v2, v3, v2
	v_mov_b32_e32 v3, s4
	ds_write_b32 v3, v2
	v_mov_b32_e32 v3, v40
	v_readlane_b32 s4, v254, 53
	v_add_u32_e32 v3, 0xff, v3
	v_and_b32_e32 v3, 0xffffff00, v3
	v_add_u32_e32 v2, v3, v2
	v_mov_b32_e32 v3, s70
	ds_write_b32 v3, v2
	v_mov_b32_e32 v3, v41
	v_add_u32_e32 v3, 0xff, v3
	v_and_b32_e32 v3, 0xffffff00, v3
	v_add_u32_e32 v2, v3, v2
	v_mov_b32_e32 v3, s4
	ds_write_b32 v3, v2
	v_mov_b32_e32 v3, v42
	v_readlane_b32 s4, v254, 54
	v_add_u32_e32 v3, 0xff, v3
	v_and_b32_e32 v3, 0xffffff00, v3
	v_add_u32_e32 v2, v3, v2
	v_mov_b32_e32 v3, s58
	ds_write_b32 v3, v2
	v_mov_b32_e32 v3, v43
	v_add_u32_e32 v3, 0xff, v3
	v_and_b32_e32 v3, 0xffffff00, v3
	v_add_u32_e32 v2, v3, v2
	v_mov_b32_e32 v3, s4
	ds_write_b32 v3, v2
	v_mov_b32_e32 v3, v44
	v_readlane_b32 s4, v254, 55
	v_add_u32_e32 v3, 0xff, v3
	v_and_b32_e32 v3, 0xffffff00, v3
	v_add_u32_e32 v2, v3, v2
	v_mov_b32_e32 v3, s76
	ds_write_b32 v3, v2
	v_mov_b32_e32 v3, v45
	v_add_u32_e32 v3, 0xff, v3
	v_and_b32_e32 v3, 0xffffff00, v3
	v_add_u32_e32 v2, v3, v2
	v_mov_b32_e32 v3, s4
	ds_write_b32 v3, v2
	v_mov_b32_e32 v3, v46
	v_readlane_b32 s4, v254, 56
	v_add_u32_e32 v3, 0xff, v3
	v_and_b32_e32 v3, 0xffffff00, v3
	v_add_u32_e32 v2, v3, v2
	v_mov_b32_e32 v3, s74
	ds_write_b32 v3, v2
	v_mov_b32_e32 v3, v47
	v_add_u32_e32 v3, 0xff, v3
	v_and_b32_e32 v3, 0xffffff00, v3
	v_add_u32_e32 v2, v3, v2
	v_mov_b32_e32 v3, s4
	ds_write_b32 v3, v2
	v_mov_b32_e32 v3, v48
	v_readlane_b32 s4, v254, 57
	v_add_u32_e32 v3, 0xff, v3
	v_and_b32_e32 v3, 0xffffff00, v3
	v_add_u32_e32 v2, v3, v2
	v_mov_b32_e32 v3, s77
	ds_write_b32 v3, v2
	v_mov_b32_e32 v3, v49
	v_add_u32_e32 v3, 0xff, v3
	v_and_b32_e32 v3, 0xffffff00, v3
	v_add_u32_e32 v2, v3, v2
	v_mov_b32_e32 v3, s4
	ds_write_b32 v3, v2
	v_mov_b32_e32 v3, v50
	v_readlane_b32 s4, v254, 58
	v_add_u32_e32 v3, 0xff, v3
	v_and_b32_e32 v3, 0xffffff00, v3
	v_add_u32_e32 v2, v3, v2
	v_mov_b32_e32 v3, s45
	ds_write_b32 v3, v2
	v_mov_b32_e32 v3, v51
	v_add_u32_e32 v3, 0xff, v3
	v_and_b32_e32 v3, 0xffffff00, v3
	v_add_u32_e32 v2, v3, v2
	v_mov_b32_e32 v3, s4
	ds_write_b32 v3, v2
	v_mov_b32_e32 v3, v52
	v_readlane_b32 s4, v254, 59
	v_add_u32_e32 v3, 0xff, v3
	v_and_b32_e32 v3, 0xffffff00, v3
	v_add_u32_e32 v2, v3, v2
	v_mov_b32_e32 v3, s37
	ds_write_b32 v3, v2
	v_mov_b32_e32 v3, v53
	v_add_u32_e32 v3, 0xff, v3
	v_and_b32_e32 v3, 0xffffff00, v3
	v_add_u32_e32 v2, v3, v2
	v_mov_b32_e32 v3, s4
	ds_write_b32 v3, v2
	v_mov_b32_e32 v3, v54
	v_readlane_b32 s4, v254, 60
	v_add_u32_e32 v3, 0xff, v3
	v_and_b32_e32 v3, 0xffffff00, v3
	v_add_u32_e32 v2, v3, v2
	v_mov_b32_e32 v3, s30
	ds_write_b32 v3, v2
	v_mov_b32_e32 v3, v55
	v_add_u32_e32 v3, 0xff, v3
	v_and_b32_e32 v3, 0xffffff00, v3
	v_add_u32_e32 v2, v3, v2
	v_mov_b32_e32 v3, s4
	ds_write_b32 v3, v2
	v_mov_b32_e32 v3, v56
	v_readlane_b32 s4, v254, 61
	v_add_u32_e32 v3, 0xff, v3
	v_and_b32_e32 v3, 0xffffff00, v3
	v_add_u32_e32 v2, v3, v2
	v_mov_b32_e32 v3, s21
	ds_write_b32 v3, v2
	v_mov_b32_e32 v3, v57
	v_add_u32_e32 v3, 0xff, v3
	v_and_b32_e32 v3, 0xffffff00, v3
	v_add_u32_e32 v2, v3, v2
	v_mov_b32_e32 v3, s4
	ds_write_b32 v3, v2
	v_mov_b32_e32 v3, v58
	v_readlane_b32 s4, v254, 62
	v_add_u32_e32 v3, 0xff, v3
	v_and_b32_e32 v3, 0xffffff00, v3
	v_add_u32_e32 v2, v3, v2
	v_mov_b32_e32 v3, s71
	ds_write_b32 v3, v2
	v_mov_b32_e32 v3, v59
	v_add_u32_e32 v3, 0xff, v3
	v_and_b32_e32 v3, 0xffffff00, v3
	v_add_u32_e32 v2, v3, v2
	v_mov_b32_e32 v3, s4
	ds_write_b32 v3, v2
	v_mov_b32_e32 v3, v60
	v_readlane_b32 s4, v254, 63
	v_add_u32_e32 v3, 0xff, v3
	v_and_b32_e32 v3, 0xffffff00, v3
	v_add_u32_e32 v2, v3, v2
	v_mov_b32_e32 v3, s75
	ds_write_b32 v3, v2
	v_mov_b32_e32 v3, v61
	v_add_u32_e32 v3, 0xff, v3
	v_and_b32_e32 v3, 0xffffff00, v3
	v_add_u32_e32 v2, v3, v2
	v_mov_b32_e32 v3, s4
	ds_write_b32 v3, v2
	v_mov_b32_e32 v3, v62
	v_readlane_b32 s4, v255, 0
	v_add_u32_e32 v3, 0xff, v3
	v_and_b32_e32 v3, 0xffffff00, v3
	v_add_u32_e32 v2, v3, v2
	v_mov_b32_e32 v3, s4
	ds_write_b32 v3, v2
	v_mov_b32_e32 v3, v63
	v_readlane_b32 s4, v255, 1
	v_add_u32_e32 v3, 0xff, v3
	v_and_b32_e32 v3, 0xffffff00, v3
	v_add_u32_e32 v2, v3, v2
	v_mov_b32_e32 v3, s4
	ds_write_b32 v3, v2

.LBB0_1070:
	s_andn2_b64 vcc, exec, s[6:7]
	s_cbranch_vccnz .LBB0_1149
	s_mov_b32 s12, s34
	s_mov_b32 s2, s31
	v_mbcnt_lo_u32_b32 v4, -1, 0
	v_mbcnt_hi_u32_b32 v4, -1, v4
	s_waitcnt vmcnt(0) lgkmcnt(0)
	v_lshl_add_u32 v188, s12, 6, v4
	v_cmp_eq_u32_e32 vcc, 0, v188
	s_barrier
	s_and_saveexec_b64 s[6:7], vcc
	s_cbranch_execz .LBB0_1073
	v_readlane_b32 s14, v255, 20
	v_readlane_b32 s15, v255, 21
	s_lshl_b32 s4, s14, 5
	s_lshl_b64 s[14:15], s[4:5], 2
	v_readlane_b32 s4, v254, 22
	s_add_u32 s26, s4, s14
	v_readlane_b32 s4, v254, 23
	s_addc_u32 s27, s4, s15
	v_readlane_b32 s4, v254, 48
	v_mov_b32_e32 v1, s97
	s_nop 0
	v_mov_b32_e32 v0, s4
	ds_write_b32 v0, v113
	global_load_dwordx4 v[32:35], v113, s[26:27] offset:0 sc1
	global_load_dwordx4 v[36:39], v113, s[26:27] offset:16 sc1
	global_load_dwordx4 v[40:43], v113, s[26:27] offset:32 sc1
	global_load_dwordx4 v[44:47], v113, s[26:27] offset:48 sc1
	global_load_dwordx4 v[48:51], v113, s[26:27] offset:64 sc1
	global_load_dwordx4 v[52:55], v113, s[26:27] offset:80 sc1
	global_load_dwordx4 v[56:59], v113, s[26:27] offset:96 sc1
	global_load_dwordx4 v[60:63], v113, s[26:27] offset:112 sc1
	s_waitcnt vmcnt(0)
	v_mov_b32_e32 v0, v32
	v_readlane_b32 s4, v254, 49
	v_add_u32_e32 v0, 0xff, v0
	v_and_b32_e32 v0, 0xffffff00, v0
	ds_write_b32 v1, v0
	v_mov_b32_e32 v1, v33
	v_add_u32_e32 v1, 0xff, v1
	v_and_b32_e32 v1, 0xffffff00, v1
	v_add_u32_e32 v0, v1, v0
	v_mov_b32_e32 v1, s4
	ds_write_b32 v1, v0
	v_mov_b32_e32 v1, v34
	v_readlane_b32 s4, v254, 50
	v_add_u32_e32 v1, 0xff, v1
	v_and_b32_e32 v1, 0xffffff00, v1
	v_add_u32_e32 v0, v1, v0
	v_mov_b32_e32 v1, s69
	ds_write_b32 v1, v0
	v_mov_b32_e32 v1, v35
	v_add_u32_e32 v1, 0xff, v1
	v_and_b32_e32 v1, 0xffffff00, v1
	v_add_u32_e32 v0, v1, v0
	v_mov_b32_e32 v1, s4
	ds_write_b32 v1, v0
	v_mov_b32_e32 v1, v36
	v_readlane_b32 s4, v254, 51
	v_add_u32_e32 v1, 0xff, v1
	v_and_b32_e32 v1, 0xffffff00, v1
	v_add_u32_e32 v0, v1, v0
	v_mov_b32_e32 v1, s36
	ds_write_b32 v1, v0
	v_mov_b32_e32 v1, v37
	v_add_u32_e32 v1, 0xff, v1
	v_and_b32_e32 v1, 0xffffff00, v1
	v_add_u32_e32 v0, v1, v0
	v_mov_b32_e32 v1, s4
	ds_write_b32 v1, v0
	v_mov_b32_e32 v1, v38
	v_readlane_b32 s4, v254, 52
	v_add_u32_e32 v1, 0xff, v1
	v_and_b32_e32 v1, 0xffffff00, v1
	v_add_u32_e32 v0, v1, v0
	v_mov_b32_e32 v1, s83
	ds_write_b32 v1, v0
	v_mov_b32_e32 v1, v39
	v_add_u32_e32 v1, 0xff, v1
	v_and_b32_e32 v1, 0xffffff00, v1
	v_add_u32_e32 v0, v1, v0
	v_mov_b32_e32 v1, s4
	ds_write_b32 v1, v0
	v_mov_b32_e32 v1, v40
	v_readlane_b32 s4, v254, 53
	v_add_u32_e32 v1, 0xff, v1
	v_and_b32_e32 v1, 0xffffff00, v1
	v_add_u32_e32 v0, v1, v0
	v_mov_b32_e32 v1, s70
	ds_write_b32 v1, v0
	v_mov_b32_e32 v1, v41
	v_add_u32_e32 v1, 0xff, v1
	v_and_b32_e32 v1, 0xffffff00, v1
	v_add_u32_e32 v0, v1, v0
	v_mov_b32_e32 v1, s4
	ds_write_b32 v1, v0
	v_mov_b32_e32 v1, v42
	v_readlane_b32 s4, v254, 54
	v_add_u32_e32 v1, 0xff, v1
	v_and_b32_e32 v1, 0xffffff00, v1
	v_add_u32_e32 v0, v1, v0
	v_mov_b32_e32 v1, s58
	ds_write_b32 v1, v0
	v_mov_b32_e32 v1, v43
	v_add_u32_e32 v1, 0xff, v1
	v_and_b32_e32 v1, 0xffffff00, v1
	v_add_u32_e32 v0, v1, v0
	v_mov_b32_e32 v1, s4
	ds_write_b32 v1, v0
	v_mov_b32_e32 v1, v44
	v_readlane_b32 s4, v254, 55
	v_add_u32_e32 v1, 0xff, v1
	v_and_b32_e32 v1, 0xffffff00, v1
	v_add_u32_e32 v0, v1, v0
	v_mov_b32_e32 v1, s76
	ds_write_b32 v1, v0
	v_mov_b32_e32 v1, v45
	v_add_u32_e32 v1, 0xff, v1
	v_and_b32_e32 v1, 0xffffff00, v1
	v_add_u32_e32 v0, v1, v0
	v_mov_b32_e32 v1, s4
	ds_write_b32 v1, v0
	v_mov_b32_e32 v1, v46
	v_readlane_b32 s4, v254, 56
	v_add_u32_e32 v1, 0xff, v1
	v_and_b32_e32 v1, 0xffffff00, v1
	v_add_u32_e32 v0, v1, v0
	v_mov_b32_e32 v1, s74
	ds_write_b32 v1, v0
	v_mov_b32_e32 v1, v47
	v_add_u32_e32 v1, 0xff, v1
	v_and_b32_e32 v1, 0xffffff00, v1
	v_add_u32_e32 v0, v1, v0
	v_mov_b32_e32 v1, s4
	ds_write_b32 v1, v0
	v_mov_b32_e32 v1, v48
	v_readlane_b32 s4, v254, 57
	v_add_u32_e32 v1, 0xff, v1
	v_and_b32_e32 v1, 0xffffff00, v1
	v_add_u32_e32 v0, v1, v0
	v_mov_b32_e32 v1, s77
	ds_write_b32 v1, v0
	v_mov_b32_e32 v1, v49
	v_add_u32_e32 v1, 0xff, v1
	v_and_b32_e32 v1, 0xffffff00, v1
	v_add_u32_e32 v0, v1, v0
	v_mov_b32_e32 v1, s4
	ds_write_b32 v1, v0
	v_mov_b32_e32 v1, v50
	v_readlane_b32 s4, v254, 58
	v_add_u32_e32 v1, 0xff, v1
	v_and_b32_e32 v1, 0xffffff00, v1
	v_add_u32_e32 v0, v1, v0
	v_mov_b32_e32 v1, s45
	ds_write_b32 v1, v0
	v_mov_b32_e32 v1, v51
	v_add_u32_e32 v1, 0xff, v1
	v_and_b32_e32 v1, 0xffffff00, v1
	v_add_u32_e32 v0, v1, v0
	v_mov_b32_e32 v1, s4
	ds_write_b32 v1, v0
	v_mov_b32_e32 v1, v52
	v_readlane_b32 s4, v254, 59
	v_add_u32_e32 v1, 0xff, v1
	v_and_b32_e32 v1, 0xffffff00, v1
	v_add_u32_e32 v0, v1, v0
	v_mov_b32_e32 v1, s37
	ds_write_b32 v1, v0
	v_mov_b32_e32 v1, v53
	v_add_u32_e32 v1, 0xff, v1
	v_and_b32_e32 v1, 0xffffff00, v1
	v_add_u32_e32 v0, v1, v0
	v_mov_b32_e32 v1, s4
	ds_write_b32 v1, v0
	v_mov_b32_e32 v1, v54
	v_readlane_b32 s4, v254, 60
	v_add_u32_e32 v1, 0xff, v1
	v_and_b32_e32 v1, 0xffffff00, v1
	v_add_u32_e32 v0, v1, v0
	v_mov_b32_e32 v1, s30
	ds_write_b32 v1, v0
	v_mov_b32_e32 v1, v55
	v_add_u32_e32 v1, 0xff, v1
	v_and_b32_e32 v1, 0xffffff00, v1
	v_add_u32_e32 v0, v1, v0
	v_mov_b32_e32 v1, s4
	ds_write_b32 v1, v0
	v_mov_b32_e32 v1, v56
	v_readlane_b32 s4, v254, 61
	v_add_u32_e32 v1, 0xff, v1
	v_and_b32_e32 v1, 0xffffff00, v1
	v_add_u32_e32 v0, v1, v0
	v_mov_b32_e32 v1, s21
	ds_write_b32 v1, v0
	v_mov_b32_e32 v1, v57
	v_add_u32_e32 v1, 0xff, v1
	v_and_b32_e32 v1, 0xffffff00, v1
	v_add_u32_e32 v0, v1, v0
	v_mov_b32_e32 v1, s4
	ds_write_b32 v1, v0
	v_mov_b32_e32 v1, v58
	v_readlane_b32 s4, v254, 62
	v_add_u32_e32 v1, 0xff, v1
	v_and_b32_e32 v1, 0xffffff00, v1
	v_add_u32_e32 v0, v1, v0
	v_mov_b32_e32 v1, s71
	ds_write_b32 v1, v0
	v_mov_b32_e32 v1, v59
	v_add_u32_e32 v1, 0xff, v1
	v_and_b32_e32 v1, 0xffffff00, v1
	v_add_u32_e32 v0, v1, v0
	v_mov_b32_e32 v1, s4
	ds_write_b32 v1, v0
	v_mov_b32_e32 v1, v60
	v_readlane_b32 s4, v254, 63
	v_add_u32_e32 v1, 0xff, v1
	v_and_b32_e32 v1, 0xffffff00, v1
	v_add_u32_e32 v0, v1, v0
	v_mov_b32_e32 v1, s75
	ds_write_b32 v1, v0
	v_mov_b32_e32 v1, v61
	v_add_u32_e32 v1, 0xff, v1
	v_and_b32_e32 v1, 0xffffff00, v1
	v_add_u32_e32 v0, v1, v0
	v_mov_b32_e32 v1, s4
	ds_write_b32 v1, v0
	v_mov_b32_e32 v1, v62
	v_readlane_b32 s4, v255, 0
	v_add_u32_e32 v1, 0xff, v1
	v_and_b32_e32 v1, 0xffffff00, v1
	v_add_u32_e32 v0, v1, v0
	v_mov_b32_e32 v1, s4
	ds_write_b32 v1, v0
	v_mov_b32_e32 v1, v63
	v_readlane_b32 s4, v255, 1
	v_add_u32_e32 v1, 0xff, v1
	v_and_b32_e32 v1, 0xffffff00, v1
	v_add_u32_e32 v0, v1, v0
	v_mov_b32_e32 v1, s4
	ds_write_b32 v1, v0

.LBB0_1150:
	s_mov_b32 s13, s34
	s_mov_b32 s12, s31
	v_mbcnt_lo_u32_b32 v8, -1, 0
	v_mbcnt_hi_u32_b32 v8, -1, v8
	s_waitcnt vmcnt(0) lgkmcnt(0)
	v_lshl_add_u32 v182, s13, 6, v8
	v_cmp_eq_u32_e32 vcc, 0, v182
	s_barrier
	s_and_saveexec_b64 s[6:7], vcc
	s_cbranch_execz .LBB0_1152
	v_readlane_b32 s14, v255, 20
	v_readlane_b32 s15, v255, 21
	s_lshl_b32 s4, s14, 5
	s_lshl_b64 s[14:15], s[4:5], 2
	v_readlane_b32 s2, v254, 22
	s_add_u32 s26, s2, s14
	v_readlane_b32 s2, v254, 23
	s_addc_u32 s27, s2, s15
	v_readlane_b32 s2, v254, 48
	v_mov_b32_e32 v1, s97
	s_nop 0
	v_mov_b32_e32 v0, s2
	ds_write_b32 v0, v113
	global_load_dwordx4 v[32:35], v113, s[26:27] offset:0 sc1
	global_load_dwordx4 v[36:39], v113, s[26:27] offset:16 sc1
	global_load_dwordx4 v[40:43], v113, s[26:27] offset:32 sc1
	global_load_dwordx4 v[44:47], v113, s[26:27] offset:48 sc1
	global_load_dwordx4 v[48:51], v113, s[26:27] offset:64 sc1
	global_load_dwordx4 v[52:55], v113, s[26:27] offset:80 sc1
	global_load_dwordx4 v[56:59], v113, s[26:27] offset:96 sc1
	global_load_dwordx4 v[60:63], v113, s[26:27] offset:112 sc1
	s_waitcnt vmcnt(0)
	v_mov_b32_e32 v0, v32
	v_readlane_b32 s2, v254, 49
	v_add_u32_e32 v0, 0xff, v0
	v_and_b32_e32 v0, 0xffffff00, v0
	ds_write_b32 v1, v0
	v_mov_b32_e32 v1, v33
	v_add_u32_e32 v1, 0xff, v1
	v_and_b32_e32 v1, 0xffffff00, v1
	v_add_u32_e32 v0, v1, v0
	v_mov_b32_e32 v1, s2
	ds_write_b32 v1, v0
	v_mov_b32_e32 v1, v34
	v_readlane_b32 s2, v254, 50
	v_add_u32_e32 v1, 0xff, v1
	v_and_b32_e32 v1, 0xffffff00, v1
	v_add_u32_e32 v0, v1, v0
	v_mov_b32_e32 v1, s69
	ds_write_b32 v1, v0
	v_mov_b32_e32 v1, v35
	v_add_u32_e32 v1, 0xff, v1
	v_and_b32_e32 v1, 0xffffff00, v1
	v_add_u32_e32 v0, v1, v0
	v_mov_b32_e32 v1, s2
	ds_write_b32 v1, v0
	v_mov_b32_e32 v1, v36
	v_readlane_b32 s2, v254, 51
	v_add_u32_e32 v1, 0xff, v1
	v_and_b32_e32 v1, 0xffffff00, v1
	v_add_u32_e32 v0, v1, v0
	v_mov_b32_e32 v1, s36
	ds_write_b32 v1, v0
	v_mov_b32_e32 v1, v37
	v_add_u32_e32 v1, 0xff, v1
	v_and_b32_e32 v1, 0xffffff00, v1
	v_add_u32_e32 v0, v1, v0
	v_mov_b32_e32 v1, s2
	ds_write_b32 v1, v0
	v_mov_b32_e32 v1, v38
	v_readlane_b32 s2, v254, 52
	v_add_u32_e32 v1, 0xff, v1
	v_and_b32_e32 v1, 0xffffff00, v1
	v_add_u32_e32 v0, v1, v0
	v_mov_b32_e32 v1, s83
	ds_write_b32 v1, v0
	v_mov_b32_e32 v1, v39
	v_add_u32_e32 v1, 0xff, v1
	v_and_b32_e32 v1, 0xffffff00, v1
	v_add_u32_e32 v0, v1, v0
	v_mov_b32_e32 v1, s2
	ds_write_b32 v1, v0
	v_mov_b32_e32 v1, v40
	v_readlane_b32 s2, v254, 53
	v_add_u32_e32 v1, 0xff, v1
	v_and_b32_e32 v1, 0xffffff00, v1
	v_add_u32_e32 v0, v1, v0
	v_mov_b32_e32 v1, s70
	ds_write_b32 v1, v0
	v_mov_b32_e32 v1, v41
	v_add_u32_e32 v1, 0xff, v1
	v_and_b32_e32 v1, 0xffffff00, v1
	v_add_u32_e32 v0, v1, v0
	v_mov_b32_e32 v1, s2
	ds_write_b32 v1, v0
	v_mov_b32_e32 v1, v42
	v_readlane_b32 s2, v254, 54
	v_add_u32_e32 v1, 0xff, v1
	v_and_b32_e32 v1, 0xffffff00, v1
	v_add_u32_e32 v0, v1, v0
	v_mov_b32_e32 v1, s58
	ds_write_b32 v1, v0
	v_mov_b32_e32 v1, v43
	v_add_u32_e32 v1, 0xff, v1
	v_and_b32_e32 v1, 0xffffff00, v1
	v_add_u32_e32 v0, v1, v0
	v_mov_b32_e32 v1, s2
	ds_write_b32 v1, v0
	v_mov_b32_e32 v1, v44
	v_readlane_b32 s2, v254, 55
	v_add_u32_e32 v1, 0xff, v1
	v_and_b32_e32 v1, 0xffffff00, v1
	v_add_u32_e32 v0, v1, v0
	v_mov_b32_e32 v1, s76
	ds_write_b32 v1, v0
	v_mov_b32_e32 v1, v45
	v_add_u32_e32 v1, 0xff, v1
	v_and_b32_e32 v1, 0xffffff00, v1
	v_add_u32_e32 v0, v1, v0
	v_mov_b32_e32 v1, s2
	ds_write_b32 v1, v0
	v_mov_b32_e32 v1, v46
	v_readlane_b32 s2, v254, 56
	v_add_u32_e32 v1, 0xff, v1
	v_and_b32_e32 v1, 0xffffff00, v1
	v_add_u32_e32 v0, v1, v0
	v_mov_b32_e32 v1, s74
	ds_write_b32 v1, v0
	v_mov_b32_e32 v1, v47
	v_add_u32_e32 v1, 0xff, v1
	v_and_b32_e32 v1, 0xffffff00, v1
	v_add_u32_e32 v0, v1, v0
	v_mov_b32_e32 v1, s2
	ds_write_b32 v1, v0
	v_mov_b32_e32 v1, v48
	v_readlane_b32 s2, v254, 57
	v_add_u32_e32 v1, 0xff, v1
	v_and_b32_e32 v1, 0xffffff00, v1
	v_add_u32_e32 v0, v1, v0
	v_mov_b32_e32 v1, s77
	ds_write_b32 v1, v0
	v_mov_b32_e32 v1, v49
	v_add_u32_e32 v1, 0xff, v1
	v_and_b32_e32 v1, 0xffffff00, v1
	v_add_u32_e32 v0, v1, v0
	v_mov_b32_e32 v1, s2
	ds_write_b32 v1, v0
	v_mov_b32_e32 v1, v50
	v_readlane_b32 s2, v254, 58
	v_add_u32_e32 v1, 0xff, v1
	v_and_b32_e32 v1, 0xffffff00, v1
	v_add_u32_e32 v0, v1, v0
	v_mov_b32_e32 v1, s45
	ds_write_b32 v1, v0
	v_mov_b32_e32 v1, v51
	v_add_u32_e32 v1, 0xff, v1
	v_and_b32_e32 v1, 0xffffff00, v1
	v_add_u32_e32 v0, v1, v0
	v_mov_b32_e32 v1, s2
	ds_write_b32 v1, v0
	v_mov_b32_e32 v1, v52
	v_readlane_b32 s2, v254, 59
	v_add_u32_e32 v1, 0xff, v1
	v_and_b32_e32 v1, 0xffffff00, v1
	v_add_u32_e32 v0, v1, v0
	v_mov_b32_e32 v1, s37
	ds_write_b32 v1, v0
	v_mov_b32_e32 v1, v53
	v_add_u32_e32 v1, 0xff, v1
	v_and_b32_e32 v1, 0xffffff00, v1
	v_add_u32_e32 v0, v1, v0
	v_mov_b32_e32 v1, s2
	ds_write_b32 v1, v0
	v_mov_b32_e32 v1, v54
	v_readlane_b32 s2, v254, 60
	v_add_u32_e32 v1, 0xff, v1
	v_and_b32_e32 v1, 0xffffff00, v1
	v_add_u32_e32 v0, v1, v0
	v_mov_b32_e32 v1, s30
	ds_write_b32 v1, v0
	v_mov_b32_e32 v1, v55
	v_add_u32_e32 v1, 0xff, v1
	v_and_b32_e32 v1, 0xffffff00, v1
	v_add_u32_e32 v0, v1, v0
	v_mov_b32_e32 v1, s2
	ds_write_b32 v1, v0
	v_mov_b32_e32 v1, v56
	v_readlane_b32 s2, v254, 61
	v_add_u32_e32 v1, 0xff, v1
	v_and_b32_e32 v1, 0xffffff00, v1
	v_add_u32_e32 v0, v1, v0
	v_mov_b32_e32 v1, s21
	ds_write_b32 v1, v0
	v_mov_b32_e32 v1, v57
	v_add_u32_e32 v1, 0xff, v1
	v_and_b32_e32 v1, 0xffffff00, v1
	v_add_u32_e32 v0, v1, v0
	v_mov_b32_e32 v1, s2
	ds_write_b32 v1, v0
	v_mov_b32_e32 v1, v58
	v_readlane_b32 s2, v254, 62
	v_add_u32_e32 v1, 0xff, v1
	v_and_b32_e32 v1, 0xffffff00, v1
	v_add_u32_e32 v0, v1, v0
	v_mov_b32_e32 v1, s71
	ds_write_b32 v1, v0
	v_mov_b32_e32 v1, v59
	v_add_u32_e32 v1, 0xff, v1
	v_and_b32_e32 v1, 0xffffff00, v1
	v_add_u32_e32 v0, v1, v0
	v_mov_b32_e32 v1, s2
	ds_write_b32 v1, v0
	v_mov_b32_e32 v1, v60
	v_readlane_b32 s2, v254, 63
	v_add_u32_e32 v1, 0xff, v1
	v_and_b32_e32 v1, 0xffffff00, v1
	v_add_u32_e32 v0, v1, v0
	v_mov_b32_e32 v1, s75
	ds_write_b32 v1, v0
	v_mov_b32_e32 v1, v61
	v_add_u32_e32 v1, 0xff, v1
	v_and_b32_e32 v1, 0xffffff00, v1
	v_add_u32_e32 v0, v1, v0
	v_mov_b32_e32 v1, s2
	ds_write_b32 v1, v0
	v_mov_b32_e32 v1, v62
	v_readlane_b32 s2, v255, 0
	v_add_u32_e32 v1, 0xff, v1
	v_and_b32_e32 v1, 0xffffff00, v1
	v_add_u32_e32 v0, v1, v0
	v_mov_b32_e32 v1, s2
	ds_write_b32 v1, v0
	v_mov_b32_e32 v1, v63
	v_readlane_b32 s2, v255, 1
	v_add_u32_e32 v1, 0xff, v1
	v_and_b32_e32 v1, 0xffffff00, v1
	v_add_u32_e32 v0, v1, v0
	v_mov_b32_e32 v1, s2
	ds_write_b32 v1, v0
